# speedup vs baseline: 1.0049x; 1.0049x over previous
.LBB1_10:
	s_or_b64 exec, exec, s[8:9]
	v_lshrrev_b32_e32 v75, 4, v113
	v_and_b32_e32 v74, 15, v0
	v_lshlrev_b32_e32 v92, 7, v74
	v_bitop3_b32 v76, v0, v75, 7 bitop3:0x6c
	v_lshl_or_b32 v108, v76, 4, v92
	s_waitcnt lgkmcnt(0)
	s_barrier
	s_load_dwordx2 s[6:7], s[0:1], 0x28
	s_load_dwordx2 s[8:9], s[0:1], 0x30
	v_and_b32_e32 v74, 15, v0
	v_bfe_u32 v75, v0, 4, 2
	v_lshrrev_b32_e32 v112, 6, v0
	v_mov_b32_e32 v115, v74
	v_bitop3_b32 v114, v115, v75, 7 bitop3:0x6c
	v_lshlrev_b32_e32 v115, 7, v115
	v_lshl_or_b32 v114, v114, 4, v115
	v_xor_b32_e32 v115, 64, v114
	v_add_u32_e32 v117, 1, v74
	v_bitop3_b32 v116, v117, v75, 7 bitop3:0x6c
	v_lshlrev_b32_e32 v117, 7, v117
	v_lshl_or_b32 v116, v116, 4, v117
	v_xor_b32_e32 v117, 64, v116
	v_add_u32_e32 v119, 2, v74
	v_bitop3_b32 v118, v119, v75, 7 bitop3:0x6c
	v_lshlrev_b32_e32 v119, 7, v119
	v_lshl_or_b32 v118, v118, 4, v119
	v_xor_b32_e32 v119, 64, v118
	v_add_u32_e32 v121, 18, v74
	v_bitop3_b32 v120, v121, v75, 7 bitop3:0x6c
	v_lshlrev_b32_e32 v121, 7, v121
	v_lshl_or_b32 v120, v120, 4, v121
	v_xor_b32_e32 v121, 64, v120
	ds_read_b128 v[76:79], v114
	ds_read_b128 v[80:83], v115
	ds_read_b128 v[84:87], v116
	ds_read_b128 v[88:91], v117
	ds_read_b128 v[92:95], v118
	ds_read_b128 v[96:99], v119
	s_waitcnt lgkmcnt(5)
	v_mfma_f32_16x16x32_f16 a[0:3], v[70:73], v[76:79], 0
	v_add_u32_e32 v123, 19, v74
	v_bitop3_b32 v122, v123, v75, 7 bitop3:0x6c
	v_lshlrev_b32_e32 v123, 7, v123
	v_lshl_or_b32 v122, v122, 4, v123
	v_xor_b32_e32 v123, 64, v122
	ds_read_b128 v[100:103], v120
	s_waitcnt lgkmcnt(5)
	v_mfma_f32_16x16x32_f16 a[0:3], v[66:69], v[80:83], a[0:3]
	ds_read_b128 v[104:107], v121
	s_waitcnt lgkmcnt(5)
	v_mfma_f32_16x16x32_f16 a[0:3], v[62:65], v[84:87], a[0:3]
	v_add_u32_e32 v125, 20, v74
	v_bitop3_b32 v124, v125, v75, 7 bitop3:0x6c
	v_lshlrev_b32_e32 v125, 7, v125
	v_lshl_or_b32 v124, v124, 4, v125
	v_xor_b32_e32 v125, 64, v124
	ds_read_b128 v[76:79], v122
	s_waitcnt lgkmcnt(5)
	v_mfma_f32_16x16x32_f16 a[0:3], v[58:61], v[88:91], a[0:3]
	ds_read_b128 v[80:83], v123
	s_waitcnt lgkmcnt(5)
	v_mfma_f32_16x16x32_f16 a[0:3], v[54:57], v[92:95], a[0:3]
	v_add_u32_e32 v115, 36, v74
	v_bitop3_b32 v114, v115, v75, 7 bitop3:0x6c
	v_lshlrev_b32_e32 v115, 7, v115
	v_lshl_or_b32 v114, v114, 4, v115
	v_xor_b32_e32 v115, 64, v114
	ds_read_b128 v[84:87], v124
	s_waitcnt lgkmcnt(5)
	v_mfma_f32_16x16x32_f16 a[0:3], v[50:53], v[96:99], a[0:3]
	ds_read_b128 v[88:91], v125
	s_waitcnt lgkmcnt(5)
	v_mfma_f32_16x16x32_f16 a[4:7], v[70:73], v[100:103], 0
	v_add_u32_e32 v117, 37, v74
	v_bitop3_b32 v116, v117, v75, 7 bitop3:0x6c
	v_mfma_f32_16x16x32_f16 a[0:3], v[46:49], v[100:103], a[0:3]
	v_lshlrev_b32_e32 v117, 7, v117
	v_lshl_or_b32 v116, v116, 4, v117
	v_xor_b32_e32 v117, 64, v116
	ds_read_b128 v[92:95], v114
	s_waitcnt lgkmcnt(5)
	v_mfma_f32_16x16x32_f16 a[4:7], v[66:69], v[104:107], a[4:7]
	v_mfma_f32_16x16x32_f16 a[0:3], v[42:45], v[104:107], a[0:3]
	ds_read_b128 v[96:99], v115
	s_waitcnt lgkmcnt(5)
	v_mfma_f32_16x16x32_f16 a[4:7], v[62:65], v[76:79], a[4:7]
	v_add_u32_e32 v119, 38, v74
	v_bitop3_b32 v118, v119, v75, 7 bitop3:0x6c
	v_mfma_f32_16x16x32_f16 a[0:3], v[38:41], v[76:79], a[0:3]
	v_lshlrev_b32_e32 v119, 7, v119
	v_lshl_or_b32 v118, v118, 4, v119
	v_xor_b32_e32 v119, 64, v118
	ds_read_b128 v[100:103], v116
	s_waitcnt lgkmcnt(5)
	v_mfma_f32_16x16x32_f16 a[4:7], v[58:61], v[80:83], a[4:7]
	v_mfma_f32_16x16x32_f16 a[0:3], v[34:37], v[80:83], a[0:3]
	ds_read_b128 v[104:107], v117
	s_waitcnt lgkmcnt(5)
	v_mfma_f32_16x16x32_f16 a[4:7], v[54:57], v[84:87], a[4:7]
	v_add_u32_e32 v121, 54, v74
	v_bitop3_b32 v120, v121, v75, 7 bitop3:0x6c
	v_mfma_f32_16x16x32_f16 a[0:3], v[30:33], v[84:87], a[0:3]
	v_lshlrev_b32_e32 v121, 7, v121
	v_lshl_or_b32 v120, v120, 4, v121
	v_xor_b32_e32 v121, 64, v120
	ds_read_b128 v[76:79], v118
	s_waitcnt lgkmcnt(5)
	v_mfma_f32_16x16x32_f16 a[4:7], v[50:53], v[88:91], a[4:7]
	v_mfma_f32_16x16x32_f16 a[0:3], v[26:29], v[88:91], a[0:3]
	ds_read_b128 v[80:83], v119
	s_waitcnt lgkmcnt(5)
	v_mfma_f32_16x16x32_f16 a[8:11], v[70:73], v[92:95], 0
	v_add_u32_e32 v123, 55, v74
	v_bitop3_b32 v122, v123, v75, 7 bitop3:0x6c
	v_mfma_f32_16x16x32_f16 a[4:7], v[46:49], v[92:95], a[4:7]
	v_lshlrev_b32_e32 v123, 7, v123
	v_lshl_or_b32 v122, v122, 4, v123
	v_mfma_f32_16x16x32_f16 a[0:3], v[22:25], v[92:95], a[0:3]
	v_xor_b32_e32 v123, 64, v122
	ds_read_b128 v[84:87], v120
	s_waitcnt lgkmcnt(5)
	v_mfma_f32_16x16x32_f16 a[8:11], v[66:69], v[96:99], a[8:11]
	v_mfma_f32_16x16x32_f16 a[4:7], v[42:45], v[96:99], a[4:7]
	v_mfma_f32_16x16x32_f16 a[0:3], v[18:21], v[96:99], a[0:3]
	ds_read_b128 v[88:91], v121
	s_waitcnt lgkmcnt(5)
	v_mfma_f32_16x16x32_f16 a[8:11], v[62:65], v[100:103], a[8:11]
	v_add_u32_e32 v125, 56, v74
	v_bitop3_b32 v124, v125, v75, 7 bitop3:0x6c
	v_mfma_f32_16x16x32_f16 a[4:7], v[38:41], v[100:103], a[4:7]
	v_lshlrev_b32_e32 v125, 7, v125
	v_lshl_or_b32 v124, v124, 4, v125
	v_mfma_f32_16x16x32_f16 a[0:3], v[14:17], v[100:103], a[0:3]
	v_xor_b32_e32 v125, 64, v124
	ds_read_b128 v[92:95], v122
	s_waitcnt lgkmcnt(5)
	v_mfma_f32_16x16x32_f16 a[8:11], v[58:61], v[104:107], a[8:11]
	v_mfma_f32_16x16x32_f16 a[4:7], v[34:37], v[104:107], a[4:7]
	v_mfma_f32_16x16x32_f16 a[0:3], v[10:13], v[104:107], a[0:3]
	ds_read_b128 v[96:99], v123
	s_waitcnt lgkmcnt(5)
	v_mfma_f32_16x16x32_f16 a[8:11], v[54:57], v[76:79], a[8:11]
	v_add_u32_e32 v115, 72, v74
	v_bitop3_b32 v114, v115, v75, 7 bitop3:0x6c
	v_mfma_f32_16x16x32_f16 a[4:7], v[30:33], v[76:79], a[4:7]
	v_lshlrev_b32_e32 v115, 7, v115
	v_lshl_or_b32 v114, v114, 4, v115
	v_mfma_f32_16x16x32_f16 a[0:3], v[6:9], v[76:79], a[0:3]
	v_xor_b32_e32 v115, 64, v114
	ds_read_b128 v[100:103], v124
	s_waitcnt lgkmcnt(5)
	v_mfma_f32_16x16x32_f16 a[8:11], v[50:53], v[80:83], a[8:11]
	v_mfma_f32_16x16x32_f16 a[4:7], v[26:29], v[80:83], a[4:7]
	v_mfma_f32_16x16x32_f16 a[0:3], v[2:5], v[80:83], a[0:3]
	ds_read_b128 v[104:107], v125
	s_waitcnt lgkmcnt(5)
	v_mfma_f32_16x16x32_f16 a[12:15], v[70:73], v[84:87], 0
	v_add_u32_e32 v117, 73, v74
	v_bitop3_b32 v116, v117, v75, 7 bitop3:0x6c
	v_mfma_f32_16x16x32_f16 a[8:11], v[46:49], v[84:87], a[8:11]
	v_lshlrev_b32_e32 v117, 7, v117
	v_lshl_or_b32 v116, v116, 4, v117
	v_mfma_f32_16x16x32_f16 a[4:7], v[22:25], v[84:87], a[4:7]
	v_xor_b32_e32 v117, 64, v116
	ds_read_b128 v[76:79], v114
	s_waitcnt lgkmcnt(5)
	v_mfma_f32_16x16x32_f16 a[12:15], v[66:69], v[88:91], a[12:15]
	v_mfma_f32_16x16x32_f16 a[8:11], v[42:45], v[88:91], a[8:11]
	v_mfma_f32_16x16x32_f16 a[4:7], v[18:21], v[88:91], a[4:7]
	ds_read_b128 v[80:83], v115
	s_waitcnt lgkmcnt(5)
	v_mfma_f32_16x16x32_f16 a[12:15], v[62:65], v[92:95], a[12:15]
	v_add_u32_e32 v119, 74, v74
	v_bitop3_b32 v118, v119, v75, 7 bitop3:0x6c
	v_mfma_f32_16x16x32_f16 a[8:11], v[38:41], v[92:95], a[8:11]
	v_lshlrev_b32_e32 v119, 7, v119
	v_lshl_or_b32 v118, v118, 4, v119
	v_mfma_f32_16x16x32_f16 a[4:7], v[14:17], v[92:95], a[4:7]
	v_xor_b32_e32 v119, 64, v118
	ds_read_b128 v[84:87], v116
	s_waitcnt lgkmcnt(5)
	v_mfma_f32_16x16x32_f16 a[12:15], v[58:61], v[96:99], a[12:15]
	v_mfma_f32_16x16x32_f16 a[8:11], v[34:37], v[96:99], a[8:11]
	v_mfma_f32_16x16x32_f16 a[4:7], v[10:13], v[96:99], a[4:7]
	ds_read_b128 v[88:91], v117
	s_waitcnt lgkmcnt(5)
	v_mfma_f32_16x16x32_f16 a[12:15], v[54:57], v[100:103], a[12:15]
	v_add_u32_e32 v121, 90, v74
	v_bitop3_b32 v120, v121, v75, 7 bitop3:0x6c
	v_mfma_f32_16x16x32_f16 a[8:11], v[30:33], v[100:103], a[8:11]
	v_lshlrev_b32_e32 v121, 7, v121
	v_lshl_or_b32 v120, v120, 4, v121
	v_mfma_f32_16x16x32_f16 a[4:7], v[6:9], v[100:103], a[4:7]
	v_xor_b32_e32 v121, 64, v120
	ds_read_b128 v[92:95], v118
	s_waitcnt lgkmcnt(5)
	v_mfma_f32_16x16x32_f16 a[12:15], v[50:53], v[104:107], a[12:15]
	v_mfma_f32_16x16x32_f16 a[8:11], v[26:29], v[104:107], a[8:11]
	v_mfma_f32_16x16x32_f16 a[4:7], v[2:5], v[104:107], a[4:7]
	ds_read_b128 v[96:99], v119
	s_waitcnt lgkmcnt(5)
	v_mfma_f32_16x16x32_f16 a[12:15], v[46:49], v[76:79], a[12:15]
	v_add_u32_e32 v123, 91, v74
	v_bitop3_b32 v122, v123, v75, 7 bitop3:0x6c
	v_mfma_f32_16x16x32_f16 a[8:11], v[22:25], v[76:79], a[8:11]
	v_lshlrev_b32_e32 v123, 7, v123
	v_lshl_or_b32 v122, v122, 4, v123
	v_xor_b32_e32 v123, 64, v122
	ds_read_b128 v[100:103], v120
	s_waitcnt lgkmcnt(5)
	v_mfma_f32_16x16x32_f16 a[12:15], v[42:45], v[80:83], a[12:15]
	v_mfma_f32_16x16x32_f16 a[8:11], v[18:21], v[80:83], a[8:11]
	ds_read_b128 v[104:107], v121
	s_waitcnt lgkmcnt(5)
	v_mfma_f32_16x16x32_f16 a[12:15], v[38:41], v[84:87], a[12:15]
	v_add_u32_e32 v125, 92, v74
	v_bitop3_b32 v124, v125, v75, 7 bitop3:0x6c
	v_mfma_f32_16x16x32_f16 a[8:11], v[14:17], v[84:87], a[8:11]
	v_lshlrev_b32_e32 v125, 7, v125
	v_lshl_or_b32 v124, v124, 4, v125
	v_xor_b32_e32 v125, 64, v124
	ds_read_b128 v[76:79], v122
	s_waitcnt lgkmcnt(5)
	v_mfma_f32_16x16x32_f16 a[12:15], v[34:37], v[88:91], a[12:15]
	v_mfma_f32_16x16x32_f16 a[8:11], v[10:13], v[88:91], a[8:11]
	ds_read_b128 v[80:83], v123
	s_waitcnt lgkmcnt(5)
	v_mfma_f32_16x16x32_f16 a[12:15], v[30:33], v[92:95], a[12:15]
	v_mfma_f32_16x16x32_f16 a[8:11], v[6:9], v[92:95], a[8:11]
	ds_read_b128 v[84:87], v124
	s_waitcnt lgkmcnt(5)
	v_mfma_f32_16x16x32_f16 a[12:15], v[26:29], v[96:99], a[12:15]
	v_mfma_f32_16x16x32_f16 a[8:11], v[2:5], v[96:99], a[8:11]
	ds_read_b128 v[88:91], v125
	s_waitcnt lgkmcnt(5)
	v_mfma_f32_16x16x32_f16 a[12:15], v[22:25], v[100:103], a[12:15]
	s_waitcnt lgkmcnt(4)
	v_mfma_f32_16x16x32_f16 a[12:15], v[18:21], v[104:107], a[12:15]
	s_waitcnt lgkmcnt(3)
	v_mfma_f32_16x16x32_f16 a[12:15], v[14:17], v[76:79], a[12:15]
	s_waitcnt lgkmcnt(2)
	v_mfma_f32_16x16x32_f16 a[12:15], v[10:13], v[80:83], a[12:15]
	s_waitcnt lgkmcnt(1)
	v_mfma_f32_16x16x32_f16 a[12:15], v[6:9], v[84:87], a[12:15]
	s_waitcnt lgkmcnt(0)
	v_mfma_f32_16x16x32_f16 a[12:15], v[2:5], v[88:91], a[12:15]
	s_lshr_b32 s3, s2, 1
	s_and_b32 s3, s3, 0x7c
	s_lshl_b32 s4, s2, 4
	s_and_b32 s4, s4, 0x70
	s_lshl_b32 s3, s3, 7
	s_add_i32 s3, s3, s4
	v_add_u32_e32 v114, s3, v74
	v_lshlrev_b32_e32 v114, 7, v114
	v_lshl_add_u32 v114, v112, 5, v114
	v_lshl_add_u32 v114, v75, 3, v114
	v_add_u32_e32 v115, 0x4000, v114
	v_add_u32_e32 v116, 0x8000, v114
	v_add_u32_e32 v117, 0xc000, v114
	v_and_b32_e32 v118, 63, v0
	v_lshlrev_b32_e32 v119, 3, v112
	s_nop 7
	v_accvgpr_read_b32 v80, a0
	v_accvgpr_read_b32 v81, a1
	v_accvgpr_read_b32 v82, a2
	v_accvgpr_read_b32 v83, a3
	v_accvgpr_read_b32 v84, a4
	v_accvgpr_read_b32 v85, a5
	v_accvgpr_read_b32 v86, a6
	v_accvgpr_read_b32 v87, a7
	v_accvgpr_read_b32 v88, a8
	v_accvgpr_read_b32 v89, a9
	v_accvgpr_read_b32 v90, a10
	v_accvgpr_read_b32 v91, a11
	v_accvgpr_read_b32 v92, a12
	v_accvgpr_read_b32 v93, a13
	v_accvgpr_read_b32 v94, a14
	v_accvgpr_read_b32 v95, a15
	v_cvt_pk_f16_f32 v100, v80, v81
	v_cvt_pk_f16_f32 v101, v82, v83
	v_cvt_pk_f16_f32 v102, v84, v85
	v_cvt_pk_f16_f32 v103, v86, v87
	v_cvt_pk_f16_f32 v104, v88, v89
	v_cvt_pk_f16_f32 v105, v90, v91
	v_cvt_pk_f16_f32 v106, v92, v93
	v_cvt_pk_f16_f32 v107, v94, v95
	s_waitcnt lgkmcnt(0)
	global_store_dwordx2 v114, v[100:101], s[6:7]
	global_store_dwordx2 v115, v[102:103], s[6:7]
	global_store_dwordx2 v116, v[104:105], s[6:7]
	global_store_dwordx2 v117, v[106:107], s[6:7]
	v_add_f32_e32 v120, v80, v81
	v_mul_f32_e32 v121, v80, v80
	v_fmac_f32_e32 v121, v81, v81
	v_add_f32_e32 v120, v120, v82
	v_fmac_f32_e32 v121, v82, v82
	v_add_f32_e32 v120, v120, v83
	v_fmac_f32_e32 v121, v83, v83
	v_add_f32_e32 v120, v120, v84
	v_fmac_f32_e32 v121, v84, v84
	v_add_f32_e32 v120, v120, v85
	v_fmac_f32_e32 v121, v85, v85
	v_add_f32_e32 v120, v120, v86
	v_fmac_f32_e32 v121, v86, v86
	v_add_f32_e32 v120, v120, v87
	v_fmac_f32_e32 v121, v87, v87
	v_add_f32_e32 v120, v120, v88
	v_fmac_f32_e32 v121, v88, v88
	v_add_f32_e32 v120, v120, v89
	v_fmac_f32_e32 v121, v89, v89
	v_add_f32_e32 v120, v120, v90
	v_fmac_f32_e32 v121, v90, v90
	v_add_f32_e32 v120, v120, v91
	v_fmac_f32_e32 v121, v91, v91
	v_add_f32_e32 v120, v120, v92
	v_fmac_f32_e32 v121, v92, v92
	v_add_f32_e32 v120, v120, v93
	v_fmac_f32_e32 v121, v93, v93
	v_add_f32_e32 v120, v120, v94
	v_fmac_f32_e32 v121, v94, v94
	v_add_f32_e32 v120, v120, v95
	v_fmac_f32_e32 v121, v95, v95
	v_mov_b32_e32 v124, 0
	v_mov_b32_e32 v125, 0
	v_cmp_eq_u32_e32 vcc, 63, v118
	s_nop 1
	v_mov_b32_dpp v122, v120 row_shr:1 row_mask:0xf bank_mask:0xf bound_ctrl:1
	v_mov_b32_dpp v123, v121 row_shr:1 row_mask:0xf bank_mask:0xf bound_ctrl:1
	v_pk_add_f32 v[120:121], v[120:121], v[122:123]
	s_nop 1
	v_mov_b32_dpp v122, v120 row_shr:2 row_mask:0xf bank_mask:0xf bound_ctrl:1
	v_mov_b32_dpp v123, v121 row_shr:2 row_mask:0xf bank_mask:0xf bound_ctrl:1
	v_pk_add_f32 v[120:121], v[120:121], v[122:123]
	s_nop 1
	v_mov_b32_dpp v122, v120 row_shr:4 row_mask:0xf bank_mask:0xf bound_ctrl:1
	v_mov_b32_dpp v123, v121 row_shr:4 row_mask:0xf bank_mask:0xf bound_ctrl:1
	v_pk_add_f32 v[120:121], v[120:121], v[122:123]
	s_nop 1
	v_mov_b32_dpp v122, v120 row_shr:8 row_mask:0xf bank_mask:0xf bound_ctrl:1
	v_mov_b32_dpp v123, v121 row_shr:8 row_mask:0xf bank_mask:0xf bound_ctrl:1
	v_pk_add_f32 v[120:121], v[120:121], v[122:123]
	v_mov_b32_e32 v122, 0
	v_mov_b32_e32 v123, 0
	s_nop 0
	v_mov_b32_dpp v122, v120 row_bcast:15 row_mask:0xa bank_mask:0xf
	v_mov_b32_dpp v123, v121 row_bcast:15 row_mask:0xa bank_mask:0xf
	v_pk_add_f32 v[120:121], v[120:121], v[122:123]
	s_nop 1
	v_mov_b32_dpp v124, v120 row_bcast:31 row_mask:0xc bank_mask:0xf
	v_mov_b32_dpp v125, v121 row_bcast:31 row_mask:0xc bank_mask:0xf
	s_and_saveexec_b64 s[4:5], vcc
	v_pk_add_f32 v[120:121], v[120:121], v[124:125]
	ds_write_b64 v119, v[120:121] offset:14080
	s_or_b64 exec, exec, s[4:5]
	v_cmp_eq_u32_e32 vcc, 0, v0
	s_waitcnt lgkmcnt(0)
	s_barrier
	s_and_saveexec_b64 s[4:5], vcc
	s_cbranch_execz .Lkh_end
	v_mov_b32_e32 v8, 0
	ds_read_b128 v[0:3], v8 offset:14080
	ds_read_b128 v[4:7], v8 offset:14096
	s_lshl_b32 s2, s2, 3
	s_add_u32 s8, s8, s2
	s_addc_u32 s9, s9, 0
	s_waitcnt lgkmcnt(0)
	v_pk_add_f32 v[0:1], v[0:1], v[2:3]
	v_pk_add_f32 v[0:1], v[0:1], v[4:5]
	v_pk_add_f32 v[0:1], v[0:1], v[6:7]
	global_store_dwordx2 v8, v[0:1], s[8:9]
